# v75 + dilated-attention loop: 32 address adds per two tiles folded into a pre-biased table base (lever: address arithmetic hoisted out of the loop)
# speedup vs baseline: 1.0035x; 1.0035x over previous
.LBB0_331:
	s_cmp_eq_u32 s83, 1
	s_cselect_b32 s0, 3, 15
	s_cselect_b32 s1, 2, 4
	s_cmp_eq_u32 s83, 0
	s_cselect_b32 s84, 0, s1
	s_cselect_b32 s20, 0, s0
	s_lshl_b32 s0, s83, 2
	s_or_b32 s89, s0, s23
	s_lshr_b32 s88, 16, s84
	s_lshl_b32 s8, s89, 7
	s_add_u32 s0, s78, s8
	s_addc_u32 s1, s79, 0
	s_and_b32 s85, s20, s76
	s_add_u32 s20, s80, s8
	v_lshl_add_u64 v[34:35], v[160:161], 0, s[8:9]
	s_addc_u32 s21, s81, 0
	s_sub_i32 s8, s82, s85
	s_ashr_i32 s90, s8, s84
	s_add_i32 s8, s90, 0xffffff80
	v_add_u32_e32 v0, s8, v174
	global_load_dwordx4 v[66:69], v[34:35], off offset:3072
	global_load_dwordx4 v[70:73], v[34:35], off offset:3104
	global_load_dwordx4 v[74:77], v[34:35], off offset:3136
	global_load_dwordx4 v[78:81], v[34:35], off offset:3168
	v_max_i32_e32 v34, 0, v0
	v_lshlrev_b32_e32 v34, s84, v34
	v_max_i32_e32 v38, -16, v0
	v_max_i32_e32 v40, 0xffffffe0, v0
	v_max_i32_e32 v0, 0xffffffd0, v0
	v_add_u32_e32 v34, s85, v34
	v_add_lshl_u32 v38, v38, 16, s84
	v_add_lshl_u32 v40, v40, 32, s84
	v_add_lshl_u32 v0, v0, 48, s84
	v_min_i32_e32 v36, 0x1fff, v34
	v_mov_b64_e32 v[34:35], s[20:21]
	v_add_u32_e32 v38, s85, v38
	v_add_u32_e32 v40, s85, v40
	v_add_u32_e32 v0, s85, v0
	v_mad_i64_i32 v[36:37], s[86:87], v36, s30, v[34:35]
	v_mov_b32_e32 v157, v1
	v_min_i32_e32 v38, 0x1fff, v38
	v_min_i32_e32 v40, 0x1fff, v40
	v_min_i32_e32 v0, 0x1fff, v0
	s_mov_b32 m0, s24
	s_waitcnt lgkmcnt(0)
	v_lshl_add_u64 v[36:37], v[36:37], 0, v[156:157]
	v_mad_i64_i32 v[38:39], s[86:87], v38, s30, v[34:35]
	v_mad_i64_i32 v[40:41], s[86:87], v40, s30, v[34:35]
	v_mad_i64_i32 v[34:35], s[86:87], v0, s30, v[34:35]
	v_add_u32_e32 v0, s90, v178
	global_load_lds_dwordx4 v[36:37], off
	v_lshl_add_u64 v[38:39], v[38:39], 0, v[156:157]
	s_mov_b32 m0, s31
	v_max_i32_e32 v0, 0, v0
	global_load_lds_dwordx4 v[38:39], off
	v_lshl_add_u64 v[40:41], v[40:41], 0, v[156:157]
	s_mov_b32 m0, s33
	v_lshlrev_b32_e32 v0, s84, v0
	global_load_lds_dwordx4 v[40:41], off
	v_lshl_add_u64 v[34:35], v[34:35], 0, v[156:157]
	s_mov_b32 m0, s34
	v_add_u32_e32 v0, s85, v0
	global_load_lds_dwordx4 v[34:35], off
	v_lshl_add_u64 v[36:37], v[36:37], 0, 64
	s_mov_b32 m0, s35
	v_min_u32_e32 v0, 0x1fff, v0
	global_load_lds_dwordx4 v[36:37], off
	v_lshl_add_u64 v[36:37], v[38:39], 0, 64
	s_mov_b32 m0, s36
	v_mul_u32_u24_e32 v0, 0xf00, v0
	global_load_lds_dwordx4 v[36:37], off
	v_lshl_add_u64 v[36:37], v[40:41], 0, 64
	s_mov_b32 m0, s37
	v_lshlrev_b32_e32 v0, 1, v0
	global_load_lds_dwordx4 v[36:37], off
	v_lshl_add_u64 v[36:37], s[0:1], 0, v[0:1]
	v_add_u32_e32 v0, s8, v173
	v_max_i32_e32 v0, 0, v0
	v_lshlrev_b32_e32 v0, s84, v0
	v_add_u32_e32 v0, s85, v0
	v_min_u32_e32 v0, 0x1fff, v0
	v_lshl_add_u64 v[34:35], v[34:35], 0, 64
	s_mov_b32 m0, s38
	v_mul_u32_u24_e32 v0, 0xf00, v0
	global_load_lds_dwordx4 v[34:35], off
	v_lshlrev_b64 v[34:35], 1, v[146:147]
	v_lshlrev_b32_e32 v0, 1, v0
	v_lshl_add_u64 v[36:37], v[36:37], 0, v[34:35]
	v_lshl_add_u64 v[38:39], s[0:1], 0, v[0:1]
	v_lshl_add_u64 v[38:39], v[38:39], 0, v[34:35]
	global_load_dwordx4 v[114:117], v[36:37], off offset:96
	global_load_dwordx4 v[134:137], v[36:37], off offset:64
	global_load_dwordx4 v[130:133], v[38:39], off offset:96
	global_load_dwordx4 v[118:121], v[38:39], off offset:64
	global_load_dwordx4 v[122:125], v[36:37], off offset:32
	global_load_dwordx4 v[142:145], v[36:37], off
	global_load_dwordx4 v[138:141], v[38:39], off offset:32
	global_load_dwordx4 v[126:129], v[38:39], off
	v_subrev_u32_e32 v0, s85, v159
	s_mul_i32 s86, s88, 31
	s_mulk_i32 s89, 0x210
	v_ashrrev_i32_e32 v0, s84, v0
	s_addk_i32 s86, 0xc0
	s_add_i32 s88, s89, 0
	v_add_u32_e32 v0, v175, v0
	s_mov_b32 s87, 2
	s_lshr_b32 s86, s86, 6
	s_add_i32 s88, s88, 0x20000
	s_add_i32 s91, s88, 0xffffff84
	v_lshl_add_u64 v[162:163], s[0:1], 0, v[34:35]
	v_lshl_add_u64 v[164:165], s[20:21], 0, v[156:157]
	v_subrev_u32_e32 v157, s90, v0

.LBB0_336:
	s_waitcnt vmcnt(0)
	v_mfma_f32_32x32x16_bf16 v[50:65], v[126:129], v[66:69], 0
	v_med3_i32 v166, v157, 31, v186
	v_lshl_add_u32 v167, v166, 2, s91
	v_add_u32_e32 v166, -1, v157
	v_med3_i32 v168, v166, -1, v185
	v_med3_i32 v166, v166, 31, v186
	v_mfma_f32_32x32x16_bf16 v[34:49], v[142:145], v[66:69], 0
	v_lshl_add_u32 v192, v166, 2, s91
	v_add_u32_e32 v166, -2, v157
	v_lshl_add_u32 v169, v168, 2, s88
	v_med3_i32 v168, v166, -1, v185
	v_med3_i32 v166, v166, 31, v186
	v_lshl_add_u32 v194, v166, 2, s91
	v_mfma_f32_32x32x16_bf16 v[50:65], v[138:141], v[70:73], v[50:65]
	v_add_u32_e32 v166, -3, v157
	v_med3_i32 v0, v157, -1, v185
	v_lshl_add_u32 v193, v168, 2, s88
	v_med3_i32 v168, v166, -1, v185
	v_med3_i32 v166, v166, 31, v186
	v_lshl_add_u32 v0, v0, 2, s88
	v_lshl_add_u32 v195, v168, 2, s88
	v_mfma_f32_32x32x16_bf16 v[34:49], v[122:125], v[70:73], v[34:49]
	v_lshl_add_u32 v196, v166, 2, s91
	ds_read_b32 v166, v0 offset:4
	ds_read_b32 v168, v167
	ds_read_b32 v167, v169 offset:4
	ds_read_b32 v169, v192
	ds_read_b32 v192, v193 offset:4
	ds_read_b32 v194, v194
	ds_read_b32 v193, v195 offset:4
	ds_read_b32 v195, v196
	v_add_u32_e32 v0, -8, v157
	v_add_u32_e32 v191, s8, v170
	s_cmp_gt_i32 s8, -1
	v_mfma_f32_32x32x16_bf16 v[50:65], v[118:121], v[74:77], v[50:65]
	v_mfma_f32_32x32x16_bf16 v[34:49], v[134:137], v[74:77], v[34:49]
	v_mfma_f32_32x32x16_bf16 v[50:65], v[130:133], v[78:81], v[50:65]
	v_mfma_f32_32x32x16_bf16 v[34:49], v[114:117], v[78:81], v[34:49]
	s_waitcnt lgkmcnt(0)
	s_nop 9
	v_add_f32_e64 v50, v50, v166
	v_add_f32_e64 v51, v51, v167
	v_pk_add_f32 v[166:167], v[34:35], v[168:169]
	v_pk_add_f32 v[34:35], v[52:53], v[192:193]
	v_add_u32_e32 v53, -9, v157
	v_med3_i32 v168, v53, -1, v185
	v_med3_i32 v53, v53, 31, v186
	v_lshl_add_u32 v192, v53, 2, s91
	v_add_u32_e32 v53, -10, v157
	v_lshl_add_u32 v169, v168, 2, s88
	v_med3_i32 v168, v53, -1, v185
	v_med3_i32 v53, v53, 31, v186
	v_pk_add_f32 v[36:37], v[36:37], v[194:195]
	v_lshl_add_u32 v194, v53, 2, s91
	v_add_u32_e32 v53, -11, v157
	v_med3_i32 v52, v0, -1, v185
	v_med3_i32 v0, v0, 31, v186
	v_lshl_add_u32 v193, v168, 2, s88
	v_med3_i32 v168, v53, -1, v185
	v_med3_i32 v53, v53, 31, v186
	v_lshl_add_u32 v52, v52, 2, s88
	v_lshl_add_u32 v195, v168, 2, s88
	v_lshl_add_u32 v0, v0, 2, s91
	v_lshl_add_u32 v196, v53, 2, s91
	ds_read_b32 v52, v52 offset:4
	ds_read_b32 v168, v0
	ds_read_b32 v53, v169 offset:4
	ds_read_b32 v169, v192
	ds_read_b32 v192, v193 offset:4
	ds_read_b32 v193, v195 offset:4
	ds_read_b32 v194, v194
	ds_read_b32 v195, v196
	s_waitcnt lgkmcnt(5)
	v_pk_add_f32 v[54:55], v[54:55], v[52:53]
	s_waitcnt lgkmcnt(4)
	v_pk_add_f32 v[52:53], v[38:39], v[168:169]
	s_waitcnt lgkmcnt(2)
	v_pk_add_f32 v[38:39], v[56:57], v[192:193]
	v_subrev_u32_e32 v57, 17, v157
	v_med3_i32 v168, v57, -1, v185
	v_med3_i32 v57, v57, 31, v186
	v_lshl_add_u32 v169, v57, 2, s91
	v_subrev_u32_e32 v57, 18, v157
	v_med3_i32 v192, v57, -1, v185
	v_med3_i32 v57, v57, 31, v186
	v_add_u32_e32 v0, -16, v157
	v_lshl_add_u32 v197, v57, 2, s91
	v_subrev_u32_e32 v57, 19, v157
	v_med3_i32 v56, v0, -1, v185
	v_med3_i32 v0, v0, 31, v186
	v_lshl_add_u32 v196, v192, 2, s88
	v_med3_i32 v192, v57, -1, v185
	v_med3_i32 v57, v57, 31, v186
	v_lshl_add_u32 v56, v56, 2, s88
	v_lshl_add_u32 v199, v192, 2, s88
	v_lshl_add_u32 v0, v0, 2, s91
	v_lshl_add_u32 v168, v168, 2, s88
	v_lshl_add_u32 v200, v57, 2, s91
	ds_read_b32 v56, v56 offset:4
	ds_read_b32 v192, v0
	ds_read_b32 v57, v168 offset:4
	ds_read_b32 v193, v169
	ds_read_b32 v196, v196 offset:4
	ds_read_b32 v198, v197
	ds_read_b32 v197, v199 offset:4
	ds_read_b32 v199, v200
	s_waitcnt lgkmcnt(5)
	v_pk_add_f32 v[58:59], v[58:59], v[56:57]
	s_waitcnt lgkmcnt(4)
	v_pk_add_f32 v[56:57], v[42:43], v[192:193]
	v_pk_add_f32 v[168:169], v[40:41], v[194:195]
	s_waitcnt lgkmcnt(1)
	v_pk_add_f32 v[40:41], v[60:61], v[196:197]
	s_waitcnt lgkmcnt(0)
	v_pk_add_f32 v[42:43], v[44:45], v[198:199]
	v_subrev_u32_e32 v45, 25, v157
	v_med3_i32 v60, v45, -1, v185
	v_med3_i32 v45, v45, 31, v186
	v_lshl_add_u32 v192, v45, 2, s91
	v_subrev_u32_e32 v45, 26, v157
	v_lshl_add_u32 v61, v60, 2, s88
	v_med3_i32 v60, v45, -1, v185
	v_med3_i32 v45, v45, 31, v186
	v_subrev_u32_e32 v0, 24, v157
	v_lshl_add_u32 v194, v45, 2, s91
	v_subrev_u32_e32 v45, 27, v157
	v_med3_i32 v44, v0, -1, v185
	v_med3_i32 v0, v0, 31, v186
	v_lshl_add_u32 v193, v60, 2, s88
	v_med3_i32 v60, v45, -1, v185
	v_med3_i32 v45, v45, 31, v186
	v_lshl_add_u32 v44, v44, 2, s88
	v_lshl_add_u32 v195, v60, 2, s88
	v_lshl_add_u32 v0, v0, 2, s91
	v_lshl_add_u32 v196, v45, 2, s91
	ds_read_b32 v44, v44 offset:4
	ds_read_b32 v60, v0
	ds_read_b32 v45, v61 offset:4
	ds_read_b32 v61, v192
	ds_read_b32 v192, v193 offset:4
	ds_read_b32 v193, v195 offset:4
	ds_read_b32 v194, v194
	ds_read_b32 v195, v196
	s_waitcnt lgkmcnt(5)
	v_pk_add_f32 v[62:63], v[62:63], v[44:45]
	s_waitcnt lgkmcnt(4)
	v_pk_add_f32 v[60:61], v[46:47], v[60:61]
	s_waitcnt lgkmcnt(2)
	v_pk_add_f32 v[44:45], v[64:65], v[192:193]
	s_waitcnt lgkmcnt(0)
	v_pk_add_f32 v[46:47], v[48:49], v[194:195]
	s_cbranch_scc1 .LBB0_338
	v_cmp_lt_i32_e32 vcc, -1, v191
	s_nop 1
	v_cndmask_b32_e32 v50, v187, v50, vcc
	v_cmp_lt_i32_e32 vcc, -2, v191
	s_nop 1
	v_cndmask_b32_e32 v51, v187, v51, vcc
	v_cmp_lt_i32_e32 vcc, -3, v191
	s_nop 1
	v_cndmask_b32_e32 v34, v187, v34, vcc
	v_cmp_lt_i32_e32 vcc, -4, v191
	s_nop 1
	v_cndmask_b32_e32 v35, v187, v35, vcc
	v_cmp_lt_i32_e32 vcc, -9, v191
	s_nop 1
	v_cndmask_b32_e32 v54, v187, v54, vcc
	v_cmp_lt_i32_e32 vcc, -10, v191
	s_nop 1
	v_cndmask_b32_e32 v55, v187, v55, vcc
	v_cmp_lt_i32_e32 vcc, -11, v191
	s_nop 1
	v_cndmask_b32_e32 v38, v187, v38, vcc
	v_cmp_lt_i32_e32 vcc, -12, v191
	s_nop 1
	v_cndmask_b32_e32 v39, v187, v39, vcc
	v_cmp_lt_i32_e32 vcc, s53, v191
	s_nop 1
	v_cndmask_b32_e32 v58, v187, v58, vcc
	v_cmp_lt_i32_e32 vcc, s52, v191
	s_nop 1
	v_cndmask_b32_e32 v59, v187, v59, vcc
	v_cmp_lt_i32_e32 vcc, s51, v191
	s_nop 1
	v_cndmask_b32_e32 v40, v187, v40, vcc
	v_cmp_lt_i32_e32 vcc, s50, v191
	s_nop 1
	v_cndmask_b32_e32 v41, v187, v41, vcc
	v_cmp_lt_i32_e32 vcc, s49, v191
	s_nop 1
	v_cndmask_b32_e32 v62, v187, v62, vcc
	v_cmp_lt_i32_e32 vcc, s48, v191
	s_nop 1
	v_cndmask_b32_e32 v63, v187, v63, vcc
	v_cmp_lt_i32_e32 vcc, s47, v191
	s_nop 1
	v_cndmask_b32_e32 v44, v187, v44, vcc
	v_cmp_lt_i32_e32 vcc, s46, v191
	s_nop 1
	v_cndmask_b32_e32 v45, v187, v45, vcc
	v_cmp_lt_i32_e32 vcc, s70, v191
	s_nop 1
	v_cndmask_b32_e32 v166, v187, v166, vcc
	v_cmp_lt_i32_e32 vcc, s69, v191
	s_nop 1
	v_cndmask_b32_e32 v167, v187, v167, vcc
	v_cmp_lt_i32_e32 vcc, s68, v191
	s_nop 1
	v_cndmask_b32_e32 v36, v187, v36, vcc
	v_cmp_lt_i32_e32 vcc, s67, v191
	s_nop 1
	v_cndmask_b32_e32 v37, v187, v37, vcc
	v_cmp_lt_i32_e32 vcc, s66, v191
	s_nop 1
	v_cndmask_b32_e32 v52, v187, v52, vcc
	v_cmp_lt_i32_e32 vcc, s65, v191
	s_nop 1
	v_cndmask_b32_e32 v53, v187, v53, vcc
	v_cmp_lt_i32_e32 vcc, s64, v191
	s_nop 1
	v_cndmask_b32_e32 v168, v187, v168, vcc
	v_cmp_lt_i32_e32 vcc, s63, v191
	s_nop 1
	v_cndmask_b32_e32 v169, v187, v169, vcc
	v_cmp_lt_i32_e32 vcc, s62, v191
	s_nop 1
	v_cndmask_b32_e32 v56, v187, v56, vcc
	v_cmp_lt_i32_e32 vcc, s61, v191
	s_nop 1
	v_cndmask_b32_e32 v57, v187, v57, vcc
	v_cmp_lt_i32_e32 vcc, s60, v191
	s_nop 1
	v_cndmask_b32_e32 v42, v187, v42, vcc
	v_cmp_lt_i32_e32 vcc, s59, v191
	s_nop 1
	v_cndmask_b32_e32 v43, v187, v43, vcc
	v_cmp_lt_i32_e32 vcc, s58, v191
	s_nop 1
	v_cndmask_b32_e32 v60, v187, v60, vcc
	v_cmp_lt_i32_e32 vcc, s57, v191
	s_nop 1
	v_cndmask_b32_e32 v61, v187, v61, vcc
	v_cmp_lt_i32_e32 vcc, s56, v191
	s_nop 1
	v_cndmask_b32_e32 v46, v187, v46, vcc
	v_cmp_lt_i32_e32 vcc, s55, v191
	s_nop 1
	v_cndmask_b32_e32 v47, v187, v47, vcc

.LBB0_347:
	v_mfma_f32_32x32x16_bf16 v[50:65], v[86:89], v[66:69], 0
	v_add_u32_e32 v167, 0xffffffbf, v157
	v_med3_i32 v168, v167, -1, v185
	v_med3_i32 v167, v167, 31, v186
	v_lshl_add_u32 v189, v167, 2, s91
	v_add_u32_e32 v167, 0xffffffbe, v157
	v_lshl_add_u32 v169, v168, 2, s88
	v_mfma_f32_32x32x16_bf16 v[34:49], v[106:109], v[66:69], 0
	v_med3_i32 v168, v167, -1, v185
	v_med3_i32 v167, v167, 31, v186
	v_subrev_u32_e32 v0, 64, v157
	v_lshl_add_u32 v195, v167, 2, s91
	v_add_u32_e32 v167, 0xffffffbd, v157
	v_med3_i32 v166, v0, -1, v185
	v_mfma_f32_32x32x16_bf16 v[50:65], v[82:85], v[70:73], v[50:65]
	v_med3_i32 v0, v0, 31, v186
	v_lshl_add_u32 v190, v168, 2, s88
	v_med3_i32 v168, v167, -1, v185
	v_med3_i32 v167, v167, 31, v186
	v_lshl_add_u32 v166, v166, 2, s88
	v_lshl_add_u32 v197, v168, 2, s88
	v_mfma_f32_32x32x16_bf16 v[34:49], v[98:101], v[70:73], v[34:49]
	v_lshl_add_u32 v0, v0, 2, s91
	v_lshl_add_u32 v198, v167, 2, s91
	ds_read_b32 v166, v166 offset:4
	ds_read_b32 v168, v0
	ds_read_b32 v167, v169 offset:4
	ds_read_b32 v169, v189
	ds_read_b32 v194, v190 offset:4
	ds_read_b32 v196, v195
	ds_read_b32 v195, v197 offset:4
	ds_read_b32 v197, v198
	v_add_u32_e32 v0, 0xffffffb8, v157
	s_add_i32 s0, s8, 64
	s_cmp_gt_i32 s0, -1
	v_mfma_f32_32x32x16_bf16 v[50:65], v[94:97], v[74:77], v[50:65]
	v_mfma_f32_32x32x16_bf16 v[34:49], v[110:113], v[74:77], v[34:49]
	v_mfma_f32_32x32x16_bf16 v[50:65], v[90:93], v[78:81], v[50:65]
	v_mfma_f32_32x32x16_bf16 v[34:49], v[102:105], v[78:81], v[34:49]
	s_waitcnt lgkmcnt(0)
	s_nop 9
	v_add_f32_e64 v50, v50, v166
	v_add_f32_e64 v51, v51, v167
	v_pk_add_f32 v[166:167], v[34:35], v[168:169]
	v_pk_add_f32 v[34:35], v[52:53], v[194:195]
	v_add_u32_e32 v53, 0xffffffb7, v157
	v_med3_i32 v168, v53, -1, v185
	v_med3_i32 v53, v53, 31, v186
	v_lshl_add_u32 v189, v53, 2, s91
	v_add_u32_e32 v53, 0xffffffb6, v157
	v_lshl_add_u32 v169, v168, 2, s88
	v_med3_i32 v168, v53, -1, v185
	v_med3_i32 v53, v53, 31, v186
	v_pk_add_f32 v[36:37], v[36:37], v[196:197]
	v_lshl_add_u32 v196, v53, 2, s91
	v_add_u32_e32 v53, 0xffffffb5, v157
	v_lshl_add_u32 v190, v168, 2, s88
	v_med3_i32 v168, v53, -1, v185
	v_med3_i32 v53, v53, 31, v186
	v_med3_i32 v52, v0, -1, v185
	v_med3_i32 v0, v0, 31, v186
	v_lshl_add_u32 v52, v52, 2, s88
	v_lshl_add_u32 v195, v168, 2, s88
	v_lshl_add_u32 v197, v53, 2, s91
	v_lshl_add_u32 v0, v0, 2, s91
	ds_read_b32 v52, v52 offset:4
	ds_read_b32 v168, v0
	ds_read_b32 v53, v169 offset:4
	ds_read_b32 v169, v189
	ds_read_b32 v194, v190 offset:4
	ds_read_b32 v195, v195 offset:4
	ds_read_b32 v196, v196
	ds_read_b32 v197, v197
	s_waitcnt lgkmcnt(0)
	v_pk_add_f32 v[54:55], v[54:55], v[52:53]
	v_pk_add_f32 v[52:53], v[38:39], v[168:169]
	v_pk_add_f32 v[38:39], v[56:57], v[194:195]
	v_add_u32_e32 v57, 0xffffffaf, v157
	v_med3_i32 v168, v57, -1, v185
	v_med3_i32 v57, v57, 31, v186
	v_lshl_add_u32 v169, v57, 2, s91
	v_add_u32_e32 v57, 0xffffffae, v157
	v_med3_i32 v189, v57, -1, v185
	v_med3_i32 v57, v57, 31, v186
	v_lshl_add_u32 v190, v57, 2, s91
	v_add_u32_e32 v57, 0xffffffad, v157
	v_add_u32_e32 v0, 0xffffffb0, v157
	v_med3_i32 v194, v57, -1, v185
	v_med3_i32 v57, v57, 31, v186
	v_med3_i32 v56, v0, -1, v185
	v_med3_i32 v0, v0, 31, v186
	v_lshl_add_u32 v56, v56, 2, s88
	v_lshl_add_u32 v199, v194, 2, s88
	v_lshl_add_u32 v201, v57, 2, s91
	v_lshl_add_u32 v0, v0, 2, s91
	v_lshl_add_u32 v168, v168, 2, s88
	v_lshl_add_u32 v189, v189, 2, s88
	ds_read_b32 v56, v56 offset:4
	ds_read_b32 v194, v0
	ds_read_b32 v57, v168 offset:4
	ds_read_b32 v195, v169
	ds_read_b32 v198, v189 offset:4
	ds_read_b32 v200, v190
	ds_read_b32 v199, v199 offset:4
	ds_read_b32 v201, v201
	s_waitcnt lgkmcnt(0)
	v_pk_add_f32 v[58:59], v[58:59], v[56:57]
	v_pk_add_f32 v[56:57], v[42:43], v[194:195]
	v_pk_add_f32 v[168:169], v[40:41], v[196:197]
	v_pk_add_f32 v[40:41], v[60:61], v[198:199]
	v_pk_add_f32 v[42:43], v[44:45], v[200:201]
	v_add_u32_e32 v45, 0xffffffa7, v157
	v_med3_i32 v60, v45, -1, v185
	v_med3_i32 v45, v45, 31, v186
	v_lshl_add_u32 v189, v45, 2, s91
	v_add_u32_e32 v45, 0xffffffa6, v157
	v_lshl_add_u32 v61, v60, 2, s88
	v_med3_i32 v60, v45, -1, v185
	v_med3_i32 v45, v45, 31, v186
	v_lshl_add_u32 v196, v45, 2, s91
	v_add_u32_e32 v45, 0xffffffa5, v157
	v_add_u32_e32 v0, 0xffffffa8, v157
	v_lshl_add_u32 v190, v60, 2, s88
	v_med3_i32 v60, v45, -1, v185
	v_med3_i32 v45, v45, 31, v186
	v_med3_i32 v44, v0, -1, v185
	v_med3_i32 v0, v0, 31, v186
	v_lshl_add_u32 v44, v44, 2, s88
	v_lshl_add_u32 v195, v60, 2, s88
	v_lshl_add_u32 v197, v45, 2, s91
	v_lshl_add_u32 v0, v0, 2, s91
	ds_read_b32 v44, v44 offset:4
	ds_read_b32 v60, v0
	ds_read_b32 v45, v61 offset:4
	ds_read_b32 v61, v189
	ds_read_b32 v194, v190 offset:4
	ds_read_b32 v195, v195 offset:4
	ds_read_b32 v196, v196
	ds_read_b32 v197, v197
	s_waitcnt lgkmcnt(0)
	v_pk_add_f32 v[62:63], v[62:63], v[44:45]
	v_pk_add_f32 v[60:61], v[46:47], v[60:61]
	v_pk_add_f32 v[44:45], v[64:65], v[194:195]
	v_pk_add_f32 v[46:47], v[48:49], v[196:197]
	s_cbranch_scc1 .LBB0_349
	v_add_u32_e32 v0, 64, v191
	v_cmp_lt_i32_e32 vcc, -1, v0
	s_nop 1
	v_cndmask_b32_e32 v50, v187, v50, vcc
	v_cmp_lt_i32_e32 vcc, -2, v0
	s_nop 1
	v_cndmask_b32_e32 v51, v187, v51, vcc
	v_cmp_lt_i32_e32 vcc, -3, v0
	s_nop 1
	v_cndmask_b32_e32 v34, v187, v34, vcc
	v_cmp_lt_i32_e32 vcc, -4, v0
	s_nop 1
	v_cndmask_b32_e32 v35, v187, v35, vcc
	v_cmp_lt_i32_e32 vcc, -9, v0
	s_nop 1
	v_cndmask_b32_e32 v54, v187, v54, vcc
	v_cmp_lt_i32_e32 vcc, -10, v0
	s_nop 1
	v_cndmask_b32_e32 v55, v187, v55, vcc
	v_cmp_lt_i32_e32 vcc, -11, v0
	s_nop 1
	v_cndmask_b32_e32 v38, v187, v38, vcc
	v_cmp_lt_i32_e32 vcc, -12, v0
	s_nop 1
	v_cndmask_b32_e32 v39, v187, v39, vcc
	v_cmp_lt_i32_e32 vcc, s53, v0
	s_nop 1
	v_cndmask_b32_e32 v58, v187, v58, vcc
	v_cmp_lt_i32_e32 vcc, s52, v0
	s_nop 1
	v_cndmask_b32_e32 v59, v187, v59, vcc
	v_cmp_lt_i32_e32 vcc, s51, v0
	s_nop 1
	v_cndmask_b32_e32 v40, v187, v40, vcc
	v_cmp_lt_i32_e32 vcc, s50, v0
	s_nop 1
	v_cndmask_b32_e32 v41, v187, v41, vcc
	v_cmp_lt_i32_e32 vcc, s49, v0
	s_nop 1
	v_cndmask_b32_e32 v62, v187, v62, vcc
	v_cmp_lt_i32_e32 vcc, s48, v0
	s_nop 1
	v_cndmask_b32_e32 v63, v187, v63, vcc
	v_cmp_lt_i32_e32 vcc, s47, v0
	s_nop 1
	v_cndmask_b32_e32 v44, v187, v44, vcc
	v_cmp_lt_i32_e32 vcc, s46, v0
	s_nop 1
	v_cndmask_b32_e32 v45, v187, v45, vcc
	v_cmp_lt_i32_e32 vcc, s70, v0
	s_nop 1
	v_cndmask_b32_e32 v166, v187, v166, vcc
	v_cmp_lt_i32_e32 vcc, s69, v0
	s_nop 1
	v_cndmask_b32_e32 v167, v187, v167, vcc
	v_cmp_lt_i32_e32 vcc, s68, v0
	s_nop 1
	v_cndmask_b32_e32 v36, v187, v36, vcc
	v_cmp_lt_i32_e32 vcc, s67, v0
	s_nop 1
	v_cndmask_b32_e32 v37, v187, v37, vcc
	v_cmp_lt_i32_e32 vcc, s66, v0
	s_nop 1
	v_cndmask_b32_e32 v52, v187, v52, vcc
	v_cmp_lt_i32_e32 vcc, s65, v0
	s_nop 1
	v_cndmask_b32_e32 v53, v187, v53, vcc
	v_cmp_lt_i32_e32 vcc, s64, v0
	s_nop 1
	v_cndmask_b32_e32 v168, v187, v168, vcc
	v_cmp_lt_i32_e32 vcc, s63, v0
	s_nop 1
	v_cndmask_b32_e32 v169, v187, v169, vcc
	v_cmp_lt_i32_e32 vcc, s62, v0
	s_nop 1
	v_cndmask_b32_e32 v56, v187, v56, vcc
	v_cmp_lt_i32_e32 vcc, s61, v0
	s_nop 1
	v_cndmask_b32_e32 v57, v187, v57, vcc
	v_cmp_lt_i32_e32 vcc, s60, v0
	s_nop 1
	v_cndmask_b32_e32 v42, v187, v42, vcc
	v_cmp_lt_i32_e32 vcc, s59, v0
	s_nop 1
	v_cndmask_b32_e32 v43, v187, v43, vcc
	v_cmp_lt_i32_e32 vcc, s58, v0
	s_nop 1
	v_cndmask_b32_e32 v60, v187, v60, vcc
	v_cmp_lt_i32_e32 vcc, s57, v0
	s_nop 1
	v_cndmask_b32_e32 v61, v187, v61, vcc
	v_cmp_lt_i32_e32 vcc, s56, v0
	s_nop 1
	v_cndmask_b32_e32 v46, v187, v46, vcc
	v_cmp_lt_i32_e32 vcc, s55, v0
	s_nop 1
	v_cndmask_b32_e32 v47, v187, v47, vcc
